# rwkv_out (executed copy): first token's bonus/gate loads issued with the other tokens' batch instead of three serialized round trips per row half
# baseline (speedup 1.0000x reference)
; #define LAS __attribute__((address_space(3)))
; __device__ __forceinline__ int lt_tid(int wv) { int ln; asm volatile("v_mbcnt_lo_u32_b32 %0, -1, 0\n\tv_mbcnt_hi_u32_b32 %0, -1, %0" : "=v"(ln)); return (wv << 6) | ln; }
; __device__ __forceinline__ void ph_rwkv_out(const Params& p, int l, LAS unsigned char* lds, const int wvid) {
;     ...
;         int unit = rnd == 0 ? bid * NWAVE + wave : (((bid & 7) == 0 && wave == 0) ? (int)gridDim.x * NWAVE + (bid >> 3) : RUN);
;         if (unit >= RUN) continue;
;         if (bal) unit = (unit >> 6) * RCH + 1 + (unit & 63);
;         const int lane = lt_tid(wvid) & 63, l31 = lane & 31, hi = lane >> 5;
;         const int bh = unit / RCH, ch = unit % RCH, b = bh >> 2, h = bh & 3, t0 = ch * 64;
;         const size_t uo = (size_t)unit * 4096;
;         const bf16_t* GTg = (const bf16_t*)(ws + WS_RWB + RW_GT) + uo; const bf16_t* YLg = (const bf16_t*)(ws + WS_RWB + RW_YL) + uo; const bf16_t* VVg = (const bf16_t*)(ob + RO_VV) + uo;
;         const u32x4* SH = (const u32x4*)(ob + RO_SH) + (size_t)unit * 512;
;         LAS unsigned char* X = lds + wave * (2 * R2_MB); LAS unsigned char* Y = X + R2_MB;
;         R2_RAW(X, VVg); R2_RAW(Y, YLg);
;         bf16x8 ga[4][2], sb[4][2]; unsigned short yl[2][2][16];
; #pragma unroll
;         for (int ks = 0; ks < 4; ++ks)
; #pragma unroll
;             for (int x = 0; x < 2; ++x) { ga[ks][x] = *(const bf16x8*)(GTg + TM(32 * x + l31, 16 * ks + 8 * hi)); sb[ks][x] = __builtin_bit_cast(bf16x8, SH[(x * 4 + ks) * 64 + lane]); }
; #pragma unroll
;         for (int rb = 0; rb < 2; ++rb)
; #pragma unroll
;             for (int cb = 0; cb < 2; ++cb)
; #pragma unroll
;                 for (int r = 0; r < 16; ++r) yl[rb][cb][r] = (unsigned short)R2_RD16(Y, 32 * rb + (r & 3) + 8 * (r >> 2) + 4 * hi, 32 * cb + l31);
.LBB0_856:
	s_mul_hi_i32 s1, s0, 0x7e07e07f
	s_lshr_b32 s6, s1, 31
	s_ashr_i32 s1, s1, 5
	s_add_i32 s8, s1, s6
	s_mul_i32 s1, s8, 0x41
	s_sub_i32 s16, s0, s1
	s_ashr_i32 s1, s0, 31
	s_and_b32 s9, s8, 3
	s_lshl_b64 s[0:1], s[0:1], 13
	s_add_u32 s6, s20, s0
	v_mbcnt_lo_u32_b32 v0, -1, 0
	v_mbcnt_hi_u32_b32 v0, -1, v0
	s_addc_u32 s7, s21, s1
	v_and_b32_e32 v34, 63, v0
	s_add_u32 s10, s30, s0
	s_waitcnt lgkmcnt(11)
	v_lshlrev_b32_e32 v90, 4, v34
	s_addc_u32 s11, s31, s1
	s_waitcnt lgkmcnt(2)
	v_or_b32_e32 v35, 0x1000, v90
	v_or_b32_e32 v37, 0x1800, v90
	global_load_dwordx4 v[2:5], v90, s[10:11]
	global_load_dwordx4 v[6:9], v90, s[10:11] offset:1024
	global_load_dwordx4 v[10:13], v90, s[10:11] offset:2048
	global_load_dwordx4 v[14:17], v90, s[10:11] offset:3072
	v_or_b32_e32 v36, 0x1400, v90
	global_load_dwordx4 v[18:21], v35, s[10:11]
	global_load_dwordx4 v[22:25], v36, s[10:11]
	v_or_b32_e32 v38, 0x1c00, v90
	global_load_dwordx4 v[26:29], v37, s[10:11]
	global_load_dwordx4 v[30:33], v38, s[10:11]
	v_lshlrev_b32_e32 v39, 4, v0
	v_bfe_u32 v40, v0, 1, 5
	v_or_b32_e32 v34, 64, v34
	v_and_b32_e32 v39, 16, v39
	v_mul_u32_u24_e32 v40, 0x90, v40
	v_lshrrev_b32_e32 v34, 1, v34
	v_add3_u32 v40, s34, v40, v39
	v_mul_u32_u24_e32 v34, 0x90, v34
	s_ashr_i32 s8, s8, 2
	v_add3_u32 v39, s34, v34, v39
	s_add_u32 s10, s28, s0
	s_addc_u32 s11, s29, s1
	s_waitcnt vmcnt(33)
	v_bfe_u32 v103, v0, 5, 1
	s_waitcnt vmcnt(28)
	v_lshlrev_b32_e32 v96, 2, v103
	s_lshl_b32 s35, s16, 6
	v_or_b32_e32 v110, 32, v96
	v_mov_b32_e32 v34, 0x5a0
	s_add_u32 s0, s2, s0
	s_waitcnt vmcnt(24)
	v_mov_b32_e32 v91, v1
	v_and_b32_e32 v100, 31, v0
	s_addc_u32 s1, s3, s1
	v_lshlrev_b32_e32 v0, 5, v100
	v_lshl_or_b32 v0, v103, 4, v0
	v_lshl_add_u64 v[94:95], s[6:7], 0, v[0:1]
	v_or_b32_e32 v98, 1, v96
	v_readlane_b32 s48, v253, 46
	v_readlane_b32 s49, v253, 47
	v_readlane_b32 s50, v253, 48
	v_readlane_b32 s51, v253, 49
	v_readlane_b32 s52, v253, 50
	v_readlane_b32 s53, v253, 51
	v_readlane_b32 s54, v253, 52
	v_readlane_b32 s55, v253, 53
	v_readlane_b32 s56, v253, 54
	v_readlane_b32 s57, v253, 55
	v_readlane_b32 s58, v253, 56
	v_readlane_b32 s59, v253, 57
	v_readlane_b32 s60, v253, 58
	v_readlane_b32 s61, v253, 59
	v_readlane_b32 s62, v253, 60
	v_readlane_b32 s63, v253, 61
	s_mov_b64 s[48:49], s[52:53]
	s_mov_b64 s[50:51], s[54:55]
	s_mov_b64 s[52:53], s[56:57]
	s_mov_b64 s[54:55], s[58:59]
	s_mov_b64 s[56:57], s[60:61]
	s_movk_i32 s70, 0x1000
	s_mov_b64 s[58:59], s[62:63]
	s_waitcnt vmcnt(7)
	ds_write_b128 v40, v[2:5]
	s_waitcnt vmcnt(6)
	ds_write_b128 v39, v[6:9]
	s_waitcnt vmcnt(5)
	ds_write_b128 v40, v[10:13] offset:32
	s_waitcnt vmcnt(4)
	ds_write_b128 v39, v[14:17] offset:32
	s_waitcnt vmcnt(3)
	ds_write_b128 v40, v[18:21] offset:64
	s_waitcnt vmcnt(2)
	ds_write_b128 v40, v[22:25] offset:4672
	s_waitcnt vmcnt(1)
	ds_write_b128 v40, v[26:29] offset:96
	s_waitcnt vmcnt(0)
	ds_write_b128 v40, v[30:33] offset:4704
	global_load_dwordx4 v[2:5], v90, s[10:11]
	global_load_dwordx4 v[6:9], v90, s[10:11] offset:1024
	global_load_dwordx4 v[10:13], v90, s[10:11] offset:2048
	global_load_dwordx4 v[14:17], v90, s[10:11] offset:3072
	global_load_dwordx4 v[18:21], v35, s[10:11]
	global_load_dwordx4 v[22:25], v36, s[10:11]
	global_load_dwordx4 v[26:29], v37, s[10:11]
	global_load_dwordx4 v[30:33], v38, s[10:11]
	v_mad_u32_u24 v37, v110, s83, v34
	v_mov_b32_e32 v34, 0xab0
	v_mad_u32_u24 v38, v110, s83, v34
	v_lshl_add_u64 v[34:35], s[0:1], 0, v[90:91]
	s_movk_i32 s10, 0x1000
	v_add_co_u32_e32 v92, vcc, s10, v34
	v_mad_u32_u24 v36, v110, s83, s83
	s_nop 0
	v_addc_co_u32_e32 v93, vcc, 0, v35, vcc
	v_add_co_u32_e32 v94, vcc, s10, v94
	s_waitcnt vmcnt(7)
	ds_write_b128 v40, v[2:5] offset:9216
	s_waitcnt vmcnt(6)
	ds_write_b128 v39, v[6:9] offset:9216
	s_waitcnt vmcnt(5)
	ds_write_b128 v40, v[10:13] offset:9248
	s_waitcnt vmcnt(4)
	ds_write_b128 v39, v[14:17] offset:9248
	s_waitcnt vmcnt(3)
	ds_write_b128 v40, v[18:21] offset:9280
	s_waitcnt vmcnt(2)
	ds_write_b128 v40, v[22:25] offset:13888
	s_waitcnt vmcnt(1)
	ds_write_b128 v40, v[26:29] offset:9312
	s_waitcnt vmcnt(0)
	ds_write_b128 v40, v[30:33] offset:13920
	global_load_dwordx4 v[20:23], v0, s[6:7]
	global_load_dwordx4 v[78:81], v0, s[6:7] offset:1024
	global_load_dwordx4 v[28:31], v90, s[0:1]
	global_load_dwordx4 v[74:77], v90, s[0:1] offset:1024
	global_load_dwordx4 v[82:85], v0, s[6:7] offset:2048
	global_load_dwordx4 v[66:69], v0, s[6:7] offset:3072
	global_load_dwordx4 v[86:89], v[92:93], off
	global_load_dwordx4 v[70:73], v[92:93], off offset:1024
	v_lshlrev_b32_e32 v0, 1, v100
	v_add_u32_e32 v111, s34, v0
	s_movk_i32 s6, 0x240
	v_mad_u32_u24 v2, v103, s6, v111
	v_mad_u32_u24 v148, v98, s83, v111
	v_mad_u32_u24 v3, v110, s83, v111
	v_add_u32_e32 v114, v111, v36
	v_add_u32_e32 v113, v111, v37
	v_add_u32_e32 v112, v111, v38
	ds_read_u16 v4, v148 offset:9216
	ds_read_u16 v5, v148 offset:9360
	ds_read_u16 v6, v148 offset:9504
	ds_read_u16 v7, v148 offset:10224
	ds_read_u16 v8, v148 offset:10288
	ds_read_u16 v9, v148 offset:9568
	ds_read_u16 v10, v148 offset:9424
	ds_read_u16 v11, v148 offset:9280
	ds_read_u16 v12, v148 offset:10368
	ds_read_u16 v13, v148 offset:10512
	ds_read_u16 v14, v148 offset:10656
	ds_read_u16 v15, v148 offset:11376
	ds_read_u16 v16, v148 offset:11440
	ds_read_u16 v17, v148 offset:10720
	ds_read_u16 v18, v148 offset:10576
	ds_read_u16 v19, v148 offset:10432
	ds_read_u16 v24, v148 offset:11520
	ds_read_u16 v25, v148 offset:11664
	ds_read_u16 v26, v148 offset:11808
	ds_read_u16 v27, v148 offset:12528
	ds_read_u16 v32, v148 offset:12592
	ds_read_u16 v33, v148 offset:11872
	ds_read_u16 v60, v148 offset:11728
	ds_read_u16 v58, v148 offset:11584
; __device__ __forceinline__ float bf2f(bf16_t b) { return __uint_as_float(((unsigned)b) << 16); }
; __device__ __forceinline__ void ph_rwkv_out(const Params& p, int l, LAS unsigned char* lds, const int wvid) {
;     ...
;                 for (int r = 0; r < 16; ++r) yl[rb][cb][r] = (unsigned short)R2_RD16(Y, 32 * rb + (r & 3) + 8 * (r >> 2) + 4 * hi, 32 * cb + l31);
;         M64 Yt;
; #pragma unroll
;         for (int rb = 0; rb < 2; ++rb)
; #pragma unroll
;             for (int cb = 0; cb < 2; ++cb)
; #pragma unroll
;                 for (int r = 0; r < 16; ++r) Yt[rb][cb][r] = bf2f(yl[rb][cb][r]);
; #pragma unroll
;         for (int ks = 0; ks < 4; ++ks)
; #pragma unroll
;             for (int rb = 0; rb < 2; ++rb)
; #pragma unroll
;                 for (int cb = 0; cb < 2; ++cb) Yt[rb][cb] = __builtin_amdgcn_mfma_f32_32x32x16_bf16(ga[ks][rb], sb[ks][cb], Yt[rb][cb], 0, 0, 0);
;         const float lg0 = p.in[I_LNXG][l * 256 + h * 64 + l31], lg1 = p.in[I_LNXG][l * 256 + h * 64 + 32 + l31], lb0 = p.in[I_LNXB][l * 256 + h * 64 + l31], lb1 = p.in[I_LNXB][l * 256 + h * 64 + 32 + l31];
; #pragma unroll
;         for (int rb = 0; rb < 2; ++rb) {
;             unsigned short v0[16], v1[16], g0[16], g1[16]; float bcv[16];
; #pragma unroll
;             for (int r = 0; r < 16; ++r) { const int t = 32 * rb + (r & 3) + 8 * (r >> 2) + 4 * hi; const int tg = min(t0 + t, LT - 1); const size_t row = (size_t)b * LT + tg;
;                 v0[r] = (unsigned short)R2_RD16(X, t, l31); v1[r] = (unsigned short)R2_RD16(X, t, 32 + l31); g0[r] = Gg[row * 256 + h * 64 + l31]; g1[r] = Gg[row * 256 + h * 64 + 32 + l31]; bcv[r] = BCg[row * 4 + h]; }
	ds_read_u16 v46, v148 offset:12672
	ds_read_u16 v48, v148 offset:12816
	ds_read_u16 v49, v148 offset:12960
	ds_read_u16 v64, v148 offset:13024
	ds_read_u16 v102, v3 offset:9216
	ds_read_u16 v104, v3 offset:9280
	ds_read_u16 v3, v148 offset:12880
	ds_read_u16 v62, v148 offset:12736
	ds_read_u16 v106, v114 offset:9216
	ds_read_u16 v107, v114 offset:9360
	ds_read_u16 v108, v114 offset:9504
	ds_read_u16 v109, v114 offset:10224
	ds_read_u16 v115, v114 offset:10288
	ds_read_u16 v116, v114 offset:9568
	ds_read_u16 v117, v114 offset:9424
	ds_read_u16 v118, v114 offset:9280
	ds_read_u16 v119, v114 offset:10368
	ds_read_u16 v120, v113 offset:9216
	ds_read_u16 v121, v113 offset:9360
	ds_read_u16 v122, v113 offset:10080
	ds_read_u16 v123, v113 offset:10144
	ds_read_u16 v124, v113 offset:9424
	ds_read_u16 v125, v113 offset:9280
	ds_read_u16 v126, v114 offset:10432
	ds_read_u16 v127, v113 offset:10224
	ds_read_u16 v128, v113 offset:10368
	ds_read_u16 v129, v112 offset:9216
	ds_read_u16 v130, v112 offset:9936
	ds_read_u16 v131, v112 offset:10000
	ds_read_u16 v132, v112 offset:9280
	ds_read_u16 v133, v113 offset:10432
	ds_read_u16 v134, v113 offset:10288
	ds_read_u16 v135, v112 offset:10080
	ds_read_u16 v136, v112 offset:10224
	ds_read_u16 v137, v112 offset:10368
	ds_read_u16 v138, v112 offset:10432
	ds_read_u16 v139, v112 offset:10288
	ds_read_u16 v140, v112 offset:10144
	ds_read_u16 v34, v2 offset:9216
	ds_read_u16 v2, v2 offset:9280
	ds_read_u16 v141, v148
	ds_read_u16 v105, v148 offset:64
	ds_read_u16 v101, v148 offset:144
	ds_read_u16 v99, v148 offset:208
	ds_read_u16 v97, v148 offset:288
	ds_read_u16 v91, v148 offset:352
	s_waitcnt lgkmcnt(14)
	v_lshlrev_b32_e32 v35, 16, v4
	s_waitcnt lgkmcnt(7)
	v_lshlrev_b32_e32 v34, 16, v34
	v_lshlrev_b32_e32 v37, 16, v6
	v_lshlrev_b32_e32 v36, 16, v5
	v_lshlrev_b32_e32 v39, 16, v12
	v_lshlrev_b32_e32 v38, 16, v7
	v_lshlrev_b32_e32 v41, 16, v14
	v_lshlrev_b32_e32 v40, 16, v13
	v_lshlrev_b32_e32 v43, 16, v24
	v_lshlrev_b32_e32 v42, 16, v15
	v_lshlrev_b32_e32 v45, 16, v26
	v_lshlrev_b32_e32 v44, 16, v25
	v_lshlrev_b32_e32 v47, 16, v46
	v_lshlrev_b32_e32 v46, 16, v27
	v_lshlrev_b32_e32 v49, 16, v49
	v_lshlrev_b32_e32 v48, 16, v48
	v_lshlrev_b32_e32 v51, 16, v11
	s_waitcnt lgkmcnt(6)
	v_lshlrev_b32_e32 v50, 16, v2
	v_lshlrev_b32_e32 v53, 16, v9
	v_lshlrev_b32_e32 v52, 16, v10
	v_lshlrev_b32_e32 v54, 16, v8
	v_lshlrev_b32_e32 v57, 16, v17
	v_lshlrev_b32_e32 v59, 16, v58
	v_lshlrev_b32_e32 v58, 16, v16
	v_lshlrev_b32_e32 v65, 16, v64
	v_lshlrev_b32_e32 v64, 16, v3
	v_lshlrev_b32_e32 v3, 16, v106
	v_lshlrev_b32_e32 v2, 16, v102
	v_lshlrev_b32_e32 v5, 16, v108
	v_lshlrev_b32_e32 v4, 16, v107
	v_lshlrev_b32_e32 v7, 16, v119
	v_lshlrev_b32_e32 v6, 16, v109
	v_lshlrev_b32_e32 v9, 16, v121
	v_lshlrev_b32_e32 v8, 16, v120
	v_lshlrev_b32_e32 v11, 16, v127
	v_lshlrev_b32_e32 v10, 16, v122
	v_lshlrev_b32_e32 v13, 16, v129
	v_lshlrev_b32_e32 v12, 16, v128
	v_lshlrev_b32_e32 v15, 16, v135
	v_lshlrev_b32_e32 v14, 16, v130
	v_lshlrev_b32_e32 v17, 16, v137
	v_lshlrev_b32_e32 v16, 16, v136
	v_lshlrev_b32_e32 v55, 16, v19
	v_lshlrev_b32_e32 v56, 16, v18
	v_lshlrev_b32_e32 v61, 16, v33
	v_lshlrev_b32_e32 v60, 16, v60
	v_lshlrev_b32_e32 v63, 16, v62
	v_lshlrev_b32_e32 v62, 16, v32
	v_lshlrev_b32_e32 v19, 16, v118
	v_lshlrev_b32_e32 v18, 16, v104
	v_lshlrev_b32_e32 v25, 16, v124
	v_lshlrev_b32_e32 v24, 16, v125
	s_waitcnt vmcnt(5)
	v_mfma_f32_32x32x16_bf16 v[34:49], v[20:23], v[28:31], v[34:49]
	v_lshlrev_b32_e32 v27, 16, v134
	v_lshlrev_b32_e32 v26, 16, v123
	v_lshlrev_b32_e32 v33, 16, v138
	v_lshlrev_b32_e32 v32, 16, v139
	v_addc_co_u32_e32 v95, vcc, 0, v95, vcc
	v_cmp_gt_u32_e32 vcc, 32, v222
	v_mfma_f32_32x32x16_bf16 v[2:17], v[78:81], v[28:31], v[2:17]
	v_lshlrev_b32_e32 v29, 16, v132
	v_lshlrev_b32_e32 v28, 16, v133
	v_lshlrev_b32_e32 v31, 16, v140
	v_lshlrev_b32_e32 v30, 16, v131
	s_waitcnt vmcnt(1)
	v_mfma_f32_32x32x16_bf16 v[50:65], v[20:23], v[86:89], v[50:65]
	v_lshlrev_b32_e32 v21, 16, v116
	v_lshlrev_b32_e32 v20, 16, v117
	v_lshlrev_b32_e32 v23, 16, v126
	v_lshlrev_b32_e32 v22, 16, v115
	s_nop 1
	v_mfma_f32_32x32x16_bf16 v[18:33], v[78:81], v[86:89], v[18:33]
	v_mfma_f32_32x32x16_bf16 v[34:49], v[82:85], v[74:77], v[34:49]
	v_mfma_f32_32x32x16_bf16 v[2:17], v[66:69], v[74:77], v[2:17]
	global_load_dwordx4 v[74:77], v[94:95], off
	s_waitcnt vmcnt(1)
	v_mfma_f32_32x32x16_bf16 v[50:65], v[82:85], v[70:73], v[50:65]
	v_mfma_f32_32x32x16_bf16 v[18:33], v[66:69], v[70:73], v[18:33]
	global_load_dwordx4 v[70:73], v90, s[0:1] offset:2048
	global_load_dwordx4 v[78:81], v[94:95], off offset:1024
	global_load_dwordx4 v[82:85], v90, s[0:1] offset:3072
	global_load_dwordx4 v[86:89], v[92:93], off offset:2048
	global_load_dwordx4 v[66:69], v[92:93], off offset:3072
	s_lshl_b32 s0, s9, 7
	s_add_u32 s6, s22, s0
	s_addc_u32 s7, s23, 0
	s_lshl_b32 s1, s9, 2
	s_add_u32 s10, s24, s1
	s_addc_u32 s11, s25, 0
	s_waitcnt vmcnt(4)
	v_mfma_f32_32x32x16_bf16 v[34:49], v[74:77], v[70:73], v[34:49]
	s_waitcnt vmcnt(1)
	v_mfma_f32_32x32x16_bf16 v[50:65], v[74:77], v[86:89], v[50:65]
	global_load_dwordx4 v[74:77], v[94:95], off offset:2048
	v_mfma_f32_32x32x16_bf16 v[2:17], v[78:81], v[70:73], v[2:17]
	global_load_dwordx4 v[70:73], v[94:95], off offset:3072
	v_mfma_f32_32x32x16_bf16 v[18:33], v[78:81], v[86:89], v[18:33]
	v_or_b32_e32 v78, s40, v100
	v_mov_b32_e32 v79, v1
	v_lshl_or_b32 v78, s9, 6, v78
	v_lshlrev_b64 v[78:79], 2, v[78:79]
	v_lshl_add_u64 v[80:81], s[54:55], 0, v[78:79]
	v_lshl_add_u64 v[78:79], s[56:57], 0, v[78:79]
	global_load_dword v109, v[80:81], off
	global_load_dword v107, v[80:81], off offset:128
	global_load_dword v108, v[78:79], off
	global_load_dword v106, v[78:79], off offset:128
	s_waitcnt vmcnt(5)
; __device__ __forceinline__ void ph_rwkv_out(const Params& p, int l, LAS unsigned char* lds, const int wvid) {
;     ...
;                 for (int cb = 0; cb < 2; ++cb) Yt[rb][cb] = __builtin_amdgcn_mfma_f32_32x32x16_bf16(ga[ks][rb], sb[ks][cb], Yt[rb][cb], 0, 0, 0);
;         const float lg0 = p.in[I_LNXG][l * 256 + h * 64 + l31], lg1 = p.in[I_LNXG][l * 256 + h * 64 + 32 + l31], lb0 = p.in[I_LNXB][l * 256 + h * 64 + l31], lb1 = p.in[I_LNXB][l * 256 + h * 64 + 32 + l31];
; #pragma unroll
;         for (int rb = 0; rb < 2; ++rb) {
;             unsigned short v0[16], v1[16], g0[16], g1[16]; float bcv[16];
; #pragma unroll
;             for (int r = 0; r < 16; ++r) { const int t = 32 * rb + (r & 3) + 8 * (r >> 2) + 4 * hi; const int tg = min(t0 + t, LT - 1); const size_t row = (size_t)b * LT + tg;
;                 v0[r] = (unsigned short)R2_RD16(X, t, l31); v1[r] = (unsigned short)R2_RD16(X, t, 32 + l31); g0[r] = Gg[row * 256 + h * 64 + l31]; g1[r] = Gg[row * 256 + h * 64 + 32 + l31]; bcv[r] = BCg[row * 4 + h]; }
	v_mfma_f32_32x32x16_bf16 v[34:49], v[74:77], v[82:85], v[34:49]
	s_mul_hi_i32 s9, s8, 0x1010
	v_mfma_f32_32x32x16_bf16 v[50:65], v[74:77], v[66:69], v[50:65]
	v_or_b32_e32 v76, s35, v96
	v_or_b32_e32 v77, s35, v98
	v_or_b32_e32 v102, 3, v76
	v_min_i32_e32 v78, 0x100f, v77
	v_or_b32_e32 v104, 2, v76
	v_min_i32_e32 v86, 0x100f, v102
	v_ashrrev_i32_e32 v79, 31, v78
	s_waitcnt vmcnt(4)
	v_mfma_f32_32x32x16_bf16 v[2:17], v[70:73], v[82:85], v[2:17]
	v_min_i32_e32 v82, 0x100f, v104
	v_ashrrev_i32_e32 v87, 31, v86
	v_lshl_add_u64 v[74:75], s[6:7], 0, v[0:1]
	v_mad_i64_i32 v[78:79], s[6:7], s8, v251, v[78:79]
	v_ashrrev_i32_e32 v83, 31, v82
	v_mad_i64_i32 v[86:87], s[6:7], s8, v251, v[86:87]
	v_lshlrev_b64 v[80:81], 9, v[78:79]
	v_mad_i64_i32 v[82:83], s[6:7], s8, v251, v[82:83]
	v_lshlrev_b64 v[88:89], 9, v[86:87]
	v_lshl_add_u64 v[80:81], v[74:75], 0, v[80:81]
	v_lshlrev_b64 v[84:85], 9, v[82:83]
	v_lshl_add_u64 v[88:89], v[74:75], 0, v[88:89]
	v_or_b32_e32 v96, 10, v76
	v_lshl_add_u64 v[78:79], v[78:79], 4, s[10:11]
	v_lshl_add_u64 v[84:85], v[74:75], 0, v[84:85]
	v_lshl_add_u64 v[82:83], v[82:83], 4, s[10:11]
	global_load_ushort v167, v[80:81], off
	global_load_ushort v165, v[80:81], off offset:64
	global_load_dword v166, v[78:79], off
	v_min_i32_e32 v196, 0x100f, v76
	v_ashrrev_i32_e32 v197, 31, v196
	v_mad_i64_i32 v[196:197], s[6:7], s8, v251, v[196:197]
	v_lshlrev_b64 v[198:199], 9, v[196:197]
	v_lshl_add_u64 v[198:199], v[74:75], 0, v[198:199]
	v_lshl_add_u64 v[196:197], v[196:197], 4, s[10:11]
	global_load_ushort v185, v[198:199], off
	global_load_ushort v186, v[198:199], off offset:64
	global_load_dword v184, v[196:197], off
	global_load_ushort v162, v[84:85], off
	global_load_ushort v160, v[84:85], off offset:64
	global_load_dword v161, v[82:83], off
	global_load_ushort v156, v[88:89], off
	global_load_ushort v155, v[88:89], off offset:64
	v_or_b32_e32 v100, 8, v76
	v_or_b32_e32 v98, 9, v76
	v_min_i32_e32 v88, 0x100f, v96
	v_min_i32_e32 v80, 0x100f, v100
	v_min_i32_e32 v84, 0x100f, v98
	v_ashrrev_i32_e32 v89, 31, v88
	v_ashrrev_i32_e32 v81, 31, v80
	v_ashrrev_i32_e32 v85, 31, v84
	v_mad_i64_i32 v[88:89], s[6:7], s8, v251, v[88:89]
	v_mad_i64_i32 v[80:81], s[6:7], s8, v251, v[80:81]
	v_mad_i64_i32 v[84:85], s[6:7], s8, v251, v[84:85]
	v_lshlrev_b64 v[92:93], 9, v[88:89]
	v_lshl_add_u64 v[78:79], v[86:87], 4, s[10:11]
	v_lshlrev_b64 v[82:83], 9, v[80:81]
	v_lshl_add_u64 v[80:81], v[80:81], 4, s[10:11]
	v_lshlrev_b64 v[86:87], 9, v[84:85]
	v_lshl_add_u64 v[84:85], v[84:85], 4, s[10:11]
	v_lshl_add_u64 v[116:117], v[74:75], 0, v[92:93]
	v_or_b32_e32 v94, 11, v76
	v_or_b32_e32 v92, 16, v76
	v_lshl_add_u64 v[82:83], v[74:75], 0, v[82:83]
	v_lshl_add_u64 v[86:87], v[74:75], 0, v[86:87]
	global_load_dword v159, v[78:79], off
	global_load_ushort v154, v[82:83], off
	global_load_ushort v152, v[82:83], off offset:64
	global_load_dword v153, v[80:81], off
	global_load_ushort v149, v[86:87], off
	global_load_ushort v146, v[86:87], off offset:64
	global_load_dword v147, v[84:85], off
	global_load_ushort v95, v[116:117], off
	v_min_i32_e32 v80, 0x100f, v94
	v_min_i32_e32 v84, 0x100f, v92
	v_ashrrev_i32_e32 v81, 31, v80
	v_ashrrev_i32_e32 v85, 31, v84
	v_mad_i64_i32 v[80:81], s[6:7], s8, v251, v[80:81]
	v_mad_i64_i32 v[84:85], s[6:7], s8, v251, v[84:85]
	v_lshlrev_b64 v[82:83], 9, v[80:81]
	v_lshlrev_b64 v[86:87], 9, v[84:85]
	v_lshl_add_u64 v[78:79], v[88:89], 4, s[10:11]
	v_lshl_add_u64 v[82:83], v[74:75], 0, v[82:83]
	v_lshl_add_u64 v[86:87], v[74:75], 0, v[86:87]
	v_or_b32_e32 v90, 17, v76
	v_or_b32_e32 v88, 18, v76
	v_lshl_add_u64 v[80:81], v[80:81], 4, s[10:11]
	v_lshl_add_u64 v[84:85], v[84:85], 4, s[10:11]
	global_load_ushort v142, v[116:117], off offset:64
	global_load_dword v143, v[78:79], off
	global_load_ushort v139, v[82:83], off
	global_load_ushort v93, v[82:83], off offset:64
	global_load_dword v137, v[80:81], off
	global_load_ushort v135, v[86:87], off
	global_load_ushort v132, v[86:87], off offset:64
	global_load_dword v133, v[84:85], off
	v_min_i32_e32 v78, 0x100f, v90
	v_min_i32_e32 v82, 0x100f, v88
	v_or_b32_e32 v86, 19, v76
	v_ashrrev_i32_e32 v79, 31, v78
	v_ashrrev_i32_e32 v83, 31, v82
	v_min_i32_e32 v116, 0x100f, v86
	v_mad_i64_i32 v[78:79], s[6:7], s8, v251, v[78:79]
	v_mad_i64_i32 v[82:83], s[6:7], s8, v251, v[82:83]
	v_ashrrev_i32_e32 v117, 31, v116
	v_lshlrev_b64 v[80:81], 9, v[78:79]
	v_lshlrev_b64 v[84:85], 9, v[82:83]
	v_mad_i64_i32 v[116:117], s[6:7], s8, v251, v[116:117]
	v_lshl_add_u64 v[80:81], v[74:75], 0, v[80:81]
	v_lshl_add_u64 v[84:85], v[74:75], 0, v[84:85]
	v_lshlrev_b64 v[118:119], 9, v[116:117]
	v_lshl_add_u64 v[78:79], v[78:79], 4, s[10:11]
	v_lshl_add_u64 v[82:83], v[82:83], 4, s[10:11]
	v_lshl_add_u64 v[118:119], v[74:75], 0, v[118:119]
	global_load_ushort v131, v[80:81], off
	global_load_ushort v89, v[80:81], off offset:64
	global_load_dword v130, v[78:79], off
	global_load_ushort v127, v[84:85], off
	global_load_ushort v87, v[84:85], off offset:64
	global_load_dword v126, v[82:83], off
	global_load_ushort v124, v[118:119], off
	s_nop 0
	global_load_ushort v85, v[118:119], off offset:64
	v_or_b32_e32 v84, 24, v76
	v_min_i32_e32 v80, 0x100f, v84
	v_ashrrev_i32_e32 v81, 31, v80
	v_mad_i64_i32 v[80:81], s[6:7], s8, v251, v[80:81]
	v_lshlrev_b64 v[82:83], 9, v[80:81]
	v_lshl_add_u64 v[78:79], v[116:117], 4, s[10:11]
	v_lshl_add_u64 v[116:117], v[74:75], 0, v[82:83]
	v_or_b32_e32 v82, 25, v76
; __device__ __forceinline__ float bf2f(bf16_t b) { return __uint_as_float(((unsigned)b) << 16); }
; __device__ __forceinline__ bf16_t f2bf(float f) { unsigned u = __float_as_uint(f); u += 0x7FFFu + ((u >> 16) & 1u); return (bf16_t)(u >> 16); }
; __device__ __forceinline__ float frsq(float x) { return __builtin_amdgcn_rsqf(x); }
; __device__ __forceinline__ void ph_rwkv_out(const Params& p, int l, LAS unsigned char* lds, const int wvid) {
;     ...
;             for (int r = 0; r < 16; ++r) { const int t = 32 * rb + (r & 3) + 8 * (r >> 2) + 4 * hi; const int tg = min(t0 + t, LT - 1); const size_t row = (size_t)b * LT + tg;
;                 v0[r] = (unsigned short)R2_RD16(X, t, l31); v1[r] = (unsigned short)R2_RD16(X, t, 32 + l31); g0[r] = Gg[row * 256 + h * 64 + l31]; g1[r] = Gg[row * 256 + h * 64 + 32 + l31]; bcv[r] = BCg[row * 4 + h]; }
; #pragma unroll
;             for (int r = 0; r < 16; ++r) { const int t = 32 * rb + (r & 3) + 8 * (r >> 2) + 4 * hi, tg = t0 + t;
;                 const float y0 = Yt[rb][0][r], y1 = Yt[rb][1][r];
;                 const float mean = half_sum32(y0 + y1) * (1.f / 64.f); const float d0 = y0 - mean, d1 = y1 - mean;
;                 const float var = half_sum32(d0 * d0 + d1 * d1) * (1.f / 64.f); const float rs = frsq(var + 64e-5f);
;                 if (tg < LT) { const size_t row = (size_t)b * LT + tg;
;                     const float o0 = (d0 * rs * lg0 + lb0 + bcv[r] * bf2f(v0[r])) * bf2f(g0[r]);
;                     const float o1 = (d1 * rs * lg1 + lb1 + bcv[r] * bf2f(v1[r])) * bf2f(g1[r]);
;                     MIX[row * D + M_C + h * 64 + l31] = f2bf(o0); MIX[row * D + M_C + h * 64 + 32 + l31] = f2bf(o1); } }
	v_lshl_add_u64 v[118:119], v[80:81], 4, s[10:11]
	v_min_i32_e32 v80, 0x100f, v82
	v_ashrrev_i32_e32 v81, 31, v80
	v_mad_i64_i32 v[80:81], s[6:7], s8, v251, v[80:81]
	v_lshlrev_b64 v[120:121], 9, v[80:81]
	v_lshl_add_u64 v[144:145], v[80:81], 4, s[10:11]
	v_or_b32_e32 v80, 26, v76
	v_lshl_add_u64 v[128:129], v[74:75], 0, v[120:121]
	v_min_i32_e32 v120, 0x100f, v80
	v_ashrrev_i32_e32 v121, 31, v120
	v_mad_i64_i32 v[150:151], s[6:7], s8, v251, v[120:121]
	v_lshlrev_b64 v[120:121], 9, v[150:151]
	v_lshl_add_u64 v[168:169], v[74:75], 0, v[120:121]
	global_load_dword v125, v[78:79], off
	global_load_ushort v123, v[116:117], off
	global_load_ushort v83, v[116:117], off offset:64
	global_load_dword v122, v[118:119], off
	global_load_ushort v121, v[128:129], off
	global_load_ushort v81, v[128:129], off offset:64
	global_load_dword v120, v[144:145], off
	global_load_ushort v79, v[168:169], off
	v_or_b32_e32 v78, 27, v76
	v_min_i32_e32 v118, 0x100f, v78
	v_ashrrev_i32_e32 v119, 31, v118
	v_mad_i64_i32 v[118:119], s[6:7], s8, v251, v[118:119]
	v_lshl_add_u64 v[116:117], v[150:151], 4, s[10:11]
	v_lshlrev_b64 v[128:129], 9, v[118:119]
	v_lshl_add_u64 v[128:129], v[74:75], 0, v[128:129]
	v_lshl_add_u64 v[144:145], v[118:119], 4, s[10:11]
	global_load_ushort v118, v[168:169], off offset:64
	global_load_dword v119, v[116:117], off
	s_nop 0
	global_load_ushort v117, v[128:129], off
	global_load_ushort v115, v[128:129], off offset:64
	global_load_dword v116, v[144:145], off
	v_mfma_f32_32x32x16_bf16 v[18:33], v[70:73], v[66:69], v[18:33]
	ds_read_u16 v169, v148 offset:1008
	ds_read_u16 v168, v148 offset:1072
	ds_read_u16 v164, v148 offset:1152
	ds_read_u16 v163, v148 offset:1216
	ds_read_u16 v158, v148 offset:1296
	ds_read_u16 v157, v148 offset:1360
	ds_read_u16 v151, v148 offset:1440
	ds_read_u16 v150, v148 offset:1504
	ds_read_u16 v145, v148 offset:2160
	ds_read_u16 v144, v148 offset:2224
	ds_read_u16 v140, v148 offset:2304
	ds_read_u16 v138, v148 offset:2368
	ds_read_u16 v136, v148 offset:2448
	ds_read_u16 v134, v148 offset:2512
	ds_read_u16 v129, v148 offset:2592
	ds_read_u16 v128, v148 offset:2656
	ds_read_u16 v73, v148 offset:3312
	ds_read_u16 v72, v148 offset:3376
	ds_read_u16 v71, v148 offset:3456
	ds_read_u16 v70, v148 offset:3520
	ds_read_u16 v69, v148 offset:3600
	ds_read_u16 v68, v148 offset:3664
	ds_read_u16 v67, v148 offset:3744
	ds_read_u16 v66, v148 offset:3808
	v_add_f32_e32 v77, v34, v50
	v_mov_b32_e32 v148, v1
	s_add_u32 s6, s18, s0
	v_add_f32_dpp v77, v77, v77 quad_perm:[1,0,3,2] row_mask:0xf bank_mask:0xf bound_ctrl:1
	s_mulk_i32 s8, 0x1010
	s_addc_u32 s7, s19, 0
	v_add_f32_dpp v77, v77, v77 quad_perm:[2,3,0,1] row_mask:0xf bank_mask:0xf bound_ctrl:1
	s_nop 1
	v_add_f32_dpp v77, v77, v77 row_half_mirror row_mask:0xf bank_mask:0xf bound_ctrl:1
	s_nop 1
	v_add_f32_dpp v77, v77, v77 row_mirror row_mask:0xf bank_mask:0xf bound_ctrl:1
	s_nop 1
	v_mov_b32_dpp v148, v77 row_bcast:15 row_mask:0xa bank_mask:0xf
	v_add_f32_e32 v77, v77, v148
	s_nop 0
	v_readlane_b32 s0, v77, 31
	v_readlane_b32 s1, v77, 63
	s_nop 0
	v_mov_b32_e32 v148, s0
	v_mov_b32_e32 v77, s1
	v_cndmask_b32_e32 v77, v77, v148, vcc
	v_fmamk_f32 v148, v77, 0xbc800000, v34
	v_fmamk_f32 v34, v77, 0xbc800000, v50
	v_mul_f32_e32 v50, v34, v34
	v_fmac_f32_e32 v50, v148, v148
	v_mov_b32_e32 v77, v1
	v_cmp_gt_i32_e64 s[0:1], s33, v76
	v_add_f32_dpp v50, v50, v50 quad_perm:[1,0,3,2] row_mask:0xf bank_mask:0xf bound_ctrl:1
	s_nop 1
	v_add_f32_dpp v50, v50, v50 quad_perm:[2,3,0,1] row_mask:0xf bank_mask:0xf bound_ctrl:1
	s_nop 1
	v_add_f32_dpp v50, v50, v50 row_half_mirror row_mask:0xf bank_mask:0xf bound_ctrl:1
	s_nop 1
	v_add_f32_dpp v50, v50, v50 row_mirror row_mask:0xf bank_mask:0xf bound_ctrl:1
	s_nop 1
	v_mov_b32_dpp v77, v50 row_bcast:15 row_mask:0xa bank_mask:0xf
	v_add_f32_e32 v50, v50, v77
	s_nop 0
	v_readlane_b32 s36, v50, 31
	v_readlane_b32 s37, v50, 63
	s_and_saveexec_b64 s[16:17], s[0:1]
	s_cbranch_execz .LBB0_858
	v_ashrrev_i32_e32 v77, 31, v76
	v_lshl_add_u64 v[170:171], s[8:9], 0, v[76:77]
	v_lshl_add_u64 v[172:173], v[170:171], 4, s[10:11]
	s_nop 0
	v_mul_u32_u24_e32 v50, 0x240, v103
	v_mov_b32_e32 v103, s37
	v_mov_b32_e32 v174, s36
	v_cndmask_b32_e32 v103, v103, v174, vcc
	v_add_u32_e32 v50, v111, v50
	v_fmamk_f32 v103, v103, 0x3c800000, v249
	v_rsq_f32_e32 v103, v103
	ds_read_u16 v174, v50
	ds_read_u16 v50, v50 offset:64
	v_lshlrev_b64 v[172:173], 9, v[170:171]
	v_mul_f32_e32 v148, v148, v103
	v_lshl_add_u64 v[172:173], v[74:75], 0, v[172:173]
	s_waitcnt vmcnt(47)
	v_fma_f32 v148, v109, v148, v108
	s_waitcnt lgkmcnt(1)
	v_lshlrev_b32_e32 v174, 16, v174
	v_mul_f32_e32 v34, v34, v103
	s_waitcnt vmcnt(46)
	v_fma_f32 v34, v107, v34, v106
	s_waitcnt lgkmcnt(0)
	v_lshlrev_b32_e32 v50, 16, v50
	v_lshlrev_b64 v[170:171], 11, v[170:171]
	v_lshl_add_u64 v[170:171], s[6:7], 0, v[170:171]
	v_lshl_add_u64 v[170:171], v[170:171], 0, v[0:1]
	s_waitcnt vmcnt(0)
	v_fmac_f32_e32 v148, v184, v174
	v_mov_b32_e32 v174, v185
	v_fmac_f32_e32 v34, v184, v50
	v_mov_b32_e32 v50, v186
	s_nop 0
	v_lshlrev_b32_e32 v174, 16, v174
	v_mul_f32_e32 v148, v148, v174
	s_nop 0
	v_lshlrev_b32_e32 v50, 16, v50
	v_mul_f32_e32 v34, v34, v50
	v_bfe_u32 v50, v148, 16, 1
	v_add3_u32 v50, v148, v50, s79
	global_store_short_d16_hi v[170:171], v50, off offset:1024
	v_bfe_u32 v50, v34, 16, 1
	v_add3_u32 v34, v34, v50, s79
	global_store_short_d16_hi v[170:171], v34, off offset:1088
